# pooling mixer output: second v_permlane32_swap level, 4 dwordx2 row-per-lane stores become 2 dwordx4
# speedup vs baseline: 1.0273x; 1.0176x over previous
.LBB0_294:
	s_cmp_lt_i32 s46, 4
	s_cselect_b64 s[0:1], -1, 0
	s_and_b64 s[38:39], s[0:1], s[4:5]
	s_andn2_b64 vcc, exec, s[38:39]
	s_cbranch_vccnz .LBB0_463
	s_mov_b64 s[34:35], s[52:53]
	s_load_dwordx4 s[28:31], s[34:35], 0xd0
	v_mov_b32_e32 v219, v0
	s_waitcnt lgkmcnt(0)
	s_add_u32 s40, s30, 0x21e00000
	s_addc_u32 s41, s31, 0
	s_cmpk_gt_i32 s78, 0x7ff
	v_and_b32_e32 v254, 63, v219
	s_cbranch_scc1 .LBB0_317
	s_waitcnt vmcnt(0)
	s_load_dwordx2 s[12:13], s[34:35], 0x30
	v_and_b32_e32 v34, 15, v219
	v_lshrrev_b32_e32 v35, 4, v219
	v_lshlrev_b32_e32 v36, 12, v35
	v_lshl_add_u32 v36, v34, 4, v36
	v_add_u32_e32 v37, 0x20000, v36
	v_add_u32_e32 v38, 0x40000, v36
	v_add_u32_e32 v39, 0x60000, v36
	v_add_u32_e32 v40, 0x80, v35
	v_min_u32_e32 v40, 0x8e, v40
	v_lshlrev_b32_e32 v40, 12, v40
	v_lshl_add_u32 v40, v34, 4, v40
	v_max_u32_e32 v41, 15, v35
	v_lshlrev_b32_e32 v41, 12, v41
	v_lshl_add_u32 v41, v34, 4, v41
	v_cmp_gt_u32_e64 s[4:5], 15, v35
	v_cmp_gt_u32_e32 vcc, 0xf0, v219
	s_mov_b64 s[6:7], vcc
	v_lshlrev_b32_e32 v42, 4, v219
	v_and_b32_e32 v43, 0x7f, v219
	v_lshlrev_b32_e32 v43, 1, v43
	s_lshr_b32 s8, s97, 1
	s_lshl_b32 s9, s8, 13
	v_add_u32_e32 v44, s9, v43
	v_add_u32_e32 v45, 0xf00, v44
	s_mul_i32 s9, s8, 0x2200
	v_add_u32_e32 v47, s9, v43
	v_add_u32_e32 v47, 0x9000, v47
	v_and_b32_e32 v48, 31, v254
	v_lshrrev_b32_e32 v49, 5, v254
	s_and_b32 s9, s97, 3
	s_lshr_b32 s10, s97, 2
	s_lshl_b32 s11, s9, 5
	v_add_u32_e32 v50, s11, v48
	v_mul_u32_u24_e32 v51, 0x110, v50
	v_lshl_add_u32 v51, v49, 4, v51
	v_add_u32_e32 v51, 0x9000, v51
	s_lshl_b32 s11, s10, 6
	v_add_u32_e32 v52, s11, v48
	v_mul_u32_u24_e32 v52, 0x110, v52
	v_lshl_add_u32 v52, v49, 4, v52
	v_add_u32_e32 v52, 0x11800, v52
	v_mul_u32_u24_e32 v53, 0x110, v35
	v_lshl_add_u32 v53, v34, 4, v53
	v_add_u32_e32 v53, 0x11800, v53
	v_lshlrev_b32_e32 v54, 10, v50
	v_add_u32_e32 v54, s11, v54
	v_lshl_add_u32 v54, v49, 4, v54
	v_mov_b32_e32 v55, 0x43e00000
	v_mov_b32_e32 v195, 0
	v_lshlrev_b32_e32 v196, 4, v49
	s_mov_b32 s100, 0xc3e00000
	s_mov_b32 s14, s78
	s_mov_b32 s15, -1
	s_mov_b32 s21, 0
	s_and_b32 s23, s14, 3
	s_lshr_b32 s24, s14, 2
	s_lshl_b32 s24, s24, 7
	s_and_b32 s25, s24, 0x7ff
	s_sub_i32 s24, s24, 15
	s_ashr_i32 s27, s24, 31
	s_mov_b32 s26, s24
	s_lshl_b64 s[26:27], s[26:27], 12
	s_add_u32 s26, s26, s28
	s_addc_u32 s27, s27, s29
	s_lshl_b32 s23, s23, 8
	s_add_u32 s26, s26, s23
	s_addc_u32 s27, s27, 0
	v_mov_b32_e32 v1, v36
	s_cmp_lg_u32 s25, 0
	s_cbranch_scc1 .Lpool_nz_56_s14
	v_mov_b32_e32 v1, v41

.Lpool_rows_16:
	s_waitcnt lgkmcnt(0)
	v_lshlrev_b32_e32 v18, 16, v18
	v_add_f32_e32 v192, v192, v18
	v_lshlrev_b32_e32 v236, 16, v236
	v_fma_f32 v193, v192, s98, -v18
	v_sub_f32_e32 v192, v192, v236
	v_lshlrev_b32_e32 v19, 16, v19
	v_add_f32_e32 v192, v192, v19
	v_lshlrev_b32_e32 v237, 16, v237
	v_fma_f32 v194, v192, s98, -v19
	v_sub_f32_e32 v192, v192, v237
	v_cvt_pk_bf16_f32 v193, v193, v194
	ds_write_b16 v47, v193 offset:4352
	ds_write_b16_d16_hi v47, v193 offset:4624
	v_lshlrev_b32_e32 v20, 16, v20
	v_add_f32_e32 v192, v192, v20
	v_lshlrev_b32_e32 v238, 16, v238
	v_fma_f32 v193, v192, s98, -v20
	v_sub_f32_e32 v192, v192, v238
	v_lshlrev_b32_e32 v21, 16, v21
	v_add_f32_e32 v192, v192, v21
	v_lshlrev_b32_e32 v239, 16, v239
	v_fma_f32 v194, v192, s98, -v21
	v_sub_f32_e32 v192, v192, v239
	v_cvt_pk_bf16_f32 v193, v193, v194
	ds_write_b16 v47, v193 offset:4896
	ds_write_b16_d16_hi v47, v193 offset:5168
	v_lshlrev_b32_e32 v22, 16, v22
	v_add_f32_e32 v192, v192, v22
	v_lshlrev_b32_e32 v240, 16, v240
	v_fma_f32 v193, v192, s98, -v22
	v_sub_f32_e32 v192, v192, v240
	v_lshlrev_b32_e32 v23, 16, v23
	v_add_f32_e32 v192, v192, v23
	v_lshlrev_b32_e32 v241, 16, v241
	v_fma_f32 v194, v192, s98, -v23
	v_sub_f32_e32 v192, v192, v241
	v_cvt_pk_bf16_f32 v193, v193, v194
	ds_write_b16 v47, v193 offset:5440
	ds_write_b16_d16_hi v47, v193 offset:5712
	v_lshlrev_b32_e32 v24, 16, v24
	v_add_f32_e32 v192, v192, v24
	v_lshlrev_b32_e32 v242, 16, v242
	v_fma_f32 v193, v192, s98, -v24
	v_sub_f32_e32 v192, v192, v242
	v_lshlrev_b32_e32 v25, 16, v25
	v_add_f32_e32 v192, v192, v25
	v_lshlrev_b32_e32 v243, 16, v243
	v_fma_f32 v194, v192, s98, -v25
	v_sub_f32_e32 v192, v192, v243
	v_cvt_pk_bf16_f32 v193, v193, v194
	ds_write_b16 v47, v193 offset:5984
	ds_write_b16_d16_hi v47, v193 offset:6256
	v_lshlrev_b32_e32 v26, 16, v26
	v_add_f32_e32 v192, v192, v26
	v_lshlrev_b32_e32 v244, 16, v244
	v_fma_f32 v193, v192, s98, -v26
	v_sub_f32_e32 v192, v192, v244
	v_lshlrev_b32_e32 v27, 16, v27
	v_add_f32_e32 v192, v192, v27
	v_lshlrev_b32_e32 v245, 16, v245
	v_fma_f32 v194, v192, s98, -v27
	v_sub_f32_e32 v192, v192, v245
	v_cvt_pk_bf16_f32 v193, v193, v194
	ds_write_b16 v47, v193 offset:6528
	ds_write_b16_d16_hi v47, v193 offset:6800
	v_lshlrev_b32_e32 v28, 16, v28
	v_add_f32_e32 v192, v192, v28
	v_lshlrev_b32_e32 v246, 16, v246
	v_fma_f32 v193, v192, s98, -v28
	v_sub_f32_e32 v192, v192, v246
	v_lshlrev_b32_e32 v29, 16, v29
	v_add_f32_e32 v192, v192, v29
	v_lshlrev_b32_e32 v247, 16, v247
	v_fma_f32 v194, v192, s98, -v29
	v_sub_f32_e32 v192, v192, v247
	v_cvt_pk_bf16_f32 v193, v193, v194
	ds_write_b16 v47, v193 offset:7072
	ds_write_b16_d16_hi v47, v193 offset:7344
	v_lshlrev_b32_e32 v30, 16, v30
	v_add_f32_e32 v192, v192, v30
	v_lshlrev_b32_e32 v248, 16, v248
	v_fma_f32 v193, v192, s98, -v30
	v_sub_f32_e32 v192, v192, v248
	v_lshlrev_b32_e32 v31, 16, v31
	v_add_f32_e32 v192, v192, v31
	v_lshlrev_b32_e32 v249, 16, v249
	v_fma_f32 v194, v192, s98, -v31
	v_sub_f32_e32 v192, v192, v249
	v_cvt_pk_bf16_f32 v193, v193, v194
	ds_write_b16 v47, v193 offset:7616
	ds_write_b16_d16_hi v47, v193 offset:7888
	v_lshlrev_b32_e32 v32, 16, v32
	v_add_f32_e32 v192, v192, v32
	v_lshlrev_b32_e32 v250, 16, v250
	v_fma_f32 v193, v192, s98, -v32
	v_sub_f32_e32 v192, v192, v250
	v_lshlrev_b32_e32 v33, 16, v33
	v_add_f32_e32 v192, v192, v33
	v_lshlrev_b32_e32 v251, 16, v251
	v_fma_f32 v194, v192, s98, -v33
	v_sub_f32_e32 v192, v192, v251
	v_cvt_pk_bf16_f32 v193, v193, v194
	ds_write_b16 v47, v193 offset:8160
	ds_write_b16_d16_hi v47, v193 offset:8432
	s_waitcnt lgkmcnt(0)
	s_barrier
	ds_read_b128 v[220:223], v51
	ds_read_b128 v[224:227], v51 offset:32
	ds_read_b128 v[228:231], v51 offset:64
	ds_read_b128 v[232:235], v51 offset:96
	ds_read_b128 v[236:239], v51 offset:128
	ds_read_b128 v[240:243], v51 offset:160
	ds_read_b128 v[244:247], v51 offset:192
	ds_read_b128 v[248:251], v51 offset:224
	s_lshl_b32 s22, s17, 10
	s_lshl_b32 s23, s16, 7
	s_add_i32 s22, s22, s23
	s_add_u32 s18, s40, s22
	s_addc_u32 s19, s41, 0
	s_waitcnt lgkmcnt(7)
	v_mfma_f32_32x32x16_bf16 v[2:17], v[128:131], v[220:223], 0
	v_mfma_f32_32x32x16_bf16 v[18:33], v[160:163], v[220:223], 0
	s_waitcnt lgkmcnt(6)
	v_mfma_f32_32x32x16_bf16 v[2:17], v[132:135], v[224:227], v[2:17]
	v_mfma_f32_32x32x16_bf16 v[18:33], v[164:167], v[224:227], v[18:33]
	s_waitcnt lgkmcnt(5)
	v_mfma_f32_32x32x16_bf16 v[2:17], v[136:139], v[228:231], v[2:17]
	v_mfma_f32_32x32x16_bf16 v[18:33], v[168:171], v[228:231], v[18:33]
	s_waitcnt lgkmcnt(4)
	v_mfma_f32_32x32x16_bf16 v[2:17], v[140:143], v[232:235], v[2:17]
	v_mfma_f32_32x32x16_bf16 v[18:33], v[172:175], v[232:235], v[18:33]
	s_waitcnt lgkmcnt(3)
	v_mfma_f32_32x32x16_bf16 v[2:17], v[144:147], v[236:239], v[2:17]
	v_mfma_f32_32x32x16_bf16 v[18:33], v[176:179], v[236:239], v[18:33]
	s_waitcnt lgkmcnt(2)
	v_mfma_f32_32x32x16_bf16 v[2:17], v[148:151], v[240:243], v[2:17]
	v_mfma_f32_32x32x16_bf16 v[18:33], v[180:183], v[240:243], v[18:33]
	s_waitcnt lgkmcnt(1)
	v_mfma_f32_32x32x16_bf16 v[2:17], v[152:155], v[244:247], v[2:17]
	v_mfma_f32_32x32x16_bf16 v[18:33], v[184:187], v[244:247], v[18:33]
	s_waitcnt lgkmcnt(0)
	v_mfma_f32_32x32x16_bf16 v[2:17], v[156:159], v[248:251], v[2:17]
	v_mfma_f32_32x32x16_bf16 v[18:33], v[188:191], v[248:251], v[18:33]
	s_add_i32 s14, s14, s72
	s_add_i32 s21, s21, 1
	s_nop 7
	s_nop 3
	v_mul_f32_e32 v2, v2, v96
	v_mul_f32_e32 v3, v3, v97
	v_mul_f32_e32 v4, v4, v98
	v_mul_f32_e32 v5, v5, v99
	v_med3_f32 v2, v2, s100, v55
	v_med3_f32 v3, v3, s100, v55
	v_med3_f32 v4, v4, s100, v55
	v_med3_f32 v5, v5, s100, v55
	v_cvt_pk_fp8_f32 v198, v2, v3
	s_nop 0
	v_cvt_pk_fp8_f32 v198, v4, v5 op_sel:[0,0,1]
	v_mul_f32_e32 v6, v6, v100
	v_mul_f32_e32 v7, v7, v101
	v_mul_f32_e32 v8, v8, v102
	v_mul_f32_e32 v9, v9, v103
	v_med3_f32 v6, v6, s100, v55
	v_med3_f32 v7, v7, s100, v55
	v_med3_f32 v8, v8, s100, v55
	v_med3_f32 v9, v9, s100, v55
	v_cvt_pk_fp8_f32 v199, v6, v7
	s_nop 0
	v_cvt_pk_fp8_f32 v199, v8, v9 op_sel:[0,0,1]
	v_mul_f32_e32 v10, v10, v104
	v_mul_f32_e32 v11, v11, v105
	v_mul_f32_e32 v12, v12, v106
	v_mul_f32_e32 v13, v13, v107
	v_med3_f32 v10, v10, s100, v55
	v_med3_f32 v11, v11, s100, v55
	v_med3_f32 v12, v12, s100, v55
	v_med3_f32 v13, v13, s100, v55
	v_cvt_pk_fp8_f32 v200, v10, v11
	s_nop 0
	v_cvt_pk_fp8_f32 v200, v12, v13 op_sel:[0,0,1]
	v_mul_f32_e32 v14, v14, v108
	v_mul_f32_e32 v15, v15, v109
	v_mul_f32_e32 v16, v16, v110
	v_mul_f32_e32 v17, v17, v111
	v_med3_f32 v14, v14, s100, v55
	v_med3_f32 v15, v15, s100, v55
	v_med3_f32 v16, v16, s100, v55
	v_med3_f32 v17, v17, s100, v55
	v_cvt_pk_fp8_f32 v201, v14, v15
	s_nop 0
	v_cvt_pk_fp8_f32 v201, v16, v17 op_sel:[0,0,1]
	v_mul_f32_e32 v18, v18, v112
	v_mul_f32_e32 v19, v19, v113
	v_mul_f32_e32 v20, v20, v114
	v_mul_f32_e32 v21, v21, v115
	v_med3_f32 v18, v18, s100, v55
	v_med3_f32 v19, v19, s100, v55
	v_med3_f32 v20, v20, s100, v55
	v_med3_f32 v21, v21, s100, v55
	v_cvt_pk_fp8_f32 v202, v18, v19
	s_nop 0
	v_cvt_pk_fp8_f32 v202, v20, v21 op_sel:[0,0,1]
	v_mul_f32_e32 v22, v22, v116
	v_mul_f32_e32 v23, v23, v117
	v_mul_f32_e32 v24, v24, v118
	v_mul_f32_e32 v25, v25, v119
	v_med3_f32 v22, v22, s100, v55
	v_med3_f32 v23, v23, s100, v55
	v_med3_f32 v24, v24, s100, v55
	v_med3_f32 v25, v25, s100, v55
	v_cvt_pk_fp8_f32 v203, v22, v23
	s_nop 0
	v_cvt_pk_fp8_f32 v203, v24, v25 op_sel:[0,0,1]
	v_mul_f32_e32 v26, v26, v120
	v_mul_f32_e32 v27, v27, v121
	v_mul_f32_e32 v28, v28, v122
	v_mul_f32_e32 v29, v29, v123
	v_med3_f32 v26, v26, s100, v55
	v_med3_f32 v27, v27, s100, v55
	v_med3_f32 v28, v28, s100, v55
	v_med3_f32 v29, v29, s100, v55
	v_cvt_pk_fp8_f32 v204, v26, v27
	s_nop 0
	v_cvt_pk_fp8_f32 v204, v28, v29 op_sel:[0,0,1]
	v_mul_f32_e32 v30, v30, v124
	v_mul_f32_e32 v31, v31, v125
	v_mul_f32_e32 v32, v32, v126
	v_mul_f32_e32 v33, v33, v127
	v_med3_f32 v30, v30, s100, v55
	v_med3_f32 v31, v31, s100, v55
	v_med3_f32 v32, v32, s100, v55
	v_med3_f32 v33, v33, s100, v55
	v_cvt_pk_fp8_f32 v205, v30, v31
	s_nop 0
	v_cvt_pk_fp8_f32 v205, v32, v33 op_sel:[0,0,1]
	s_nop 1
	v_permlane32_swap_b32_e32 v198, v199
	v_permlane32_swap_b32_e32 v200, v201
	v_permlane32_swap_b32_e32 v202, v203
	v_permlane32_swap_b32_e32 v204, v205
	s_nop 1
	v_permlane32_swap_b32_e32 v198, v200
	v_permlane32_swap_b32_e32 v199, v201
	v_permlane32_swap_b32_e32 v202, v204
	v_permlane32_swap_b32_e32 v203, v205
	s_nop 1
	global_store_dwordx4 v54, v[198:201], s[18:19]
	global_store_dwordx4 v54, v[202:205], s[18:19] offset:32
	s_cmpk_lt_u32 s14, 0x800
	s_cbranch_scc1 .Lpool_unit
